# V phase: y^T stores issued write-through (sc0 sc1) so the V->LN2 barrier's L2 write-back has little left to flush
# speedup vs baseline: 1.0042x; 1.0042x over previous
.LBB0_956:
	s_and_b32 s8, s3, 0x78
	s_add_i32 s8, s8, s4
	s_ashr_i32 s9, s8, 31
	s_lshl_b64 s[10:11], s[8:9], 15
	s_add_u32 s10, s12, s10
	s_addc_u32 s11, s13, s11
	s_and_b32 s17, s16, 0x1000
	s_lshl_b32 s17, s17, 2
	s_add_u32 s10, s10, s17
	s_addc_u32 s11, s11, 0
	s_add_u32 s62, s10, s6
	s_addc_u32 s63, s11, s7
	s_add_u32 s64, s10, s14
	s_addc_u32 s65, s11, 0
	s_mov_b32 s17, s18
	s_nop 0
	global_load_dword v104, v2, s[62:63] offset:256
	global_load_dword v106, v2, s[62:63] offset:512
	global_load_dword v108, v2, s[62:63] offset:768
	global_load_dword v110, v2, s[62:63] offset:1024
	global_load_dword v112, v2, s[62:63] offset:1280
	global_load_dword v114, v2, s[62:63] offset:1536
	global_load_dword v98, v2, s[62:63] offset:1792
	global_load_dword v100, v2, s[62:63] offset:2048
	global_load_dword v116, v2, s[64:65] offset:-4096
	global_load_dword v102, v2, s[62:63] offset:2304
	global_load_dword v78, v2, s[62:63] offset:2560
	global_load_dword v80, v2, s[62:63] offset:2816
	global_load_dword v82, v2, s[62:63] offset:3072
	global_load_dword v84, v2, s[62:63] offset:3328
	global_load_dword v86, v2, s[62:63] offset:3584
	global_load_dword v88, v2, s[62:63] offset:3840
	global_load_dword v90, v2, s[64:65]
	global_load_dword v92, v2, s[64:65] offset:256
	global_load_dword v94, v2, s[64:65] offset:512
	global_load_dword v96, v2, s[64:65] offset:768
	global_load_dword v76, v2, s[64:65] offset:1024
	global_load_dword v77, v2, s[64:65] offset:1280
	global_load_dword v56, v2, s[64:65] offset:1536
	global_load_dword v57, v2, s[64:65] offset:1792
	global_load_dword v58, v2, s[64:65] offset:2048
	global_load_dword v59, v2, s[64:65] offset:2304
	global_load_dword v60, v2, s[64:65] offset:2560
	global_load_dword v61, v2, s[64:65] offset:2816
	global_load_dword v62, v2, s[64:65] offset:3072
	global_load_dword v63, v2, s[64:65] offset:3328
	global_load_dword v54, v2, s[64:65] offset:3584
	global_load_dword v55, v2, s[64:65] offset:3840
	s_waitcnt vmcnt(56)
	v_and_b32_e32 v9, 0x1fff8, v64
	v_and_b32_e32 v11, 0x1fff8, v66
	v_and_b32_e32 v13, 0x1fff8, v68
	v_and_b32_e32 v15, 0x1fff8, v70
	ds_read_b64 v[126:127], v9
	ds_read_b64 v[128:129], v11
	ds_read_b64 v[130:131], v13
	ds_read_b64 v[132:133], v15
	v_and_b32_e32 v9, 0x1fff8, v72
	v_and_b32_e32 v11, 0x1fff8, v74
	v_and_b32_e32 v13, 0x1fff8, v48
	v_and_b32_e32 v15, 0x1fff8, v50
	ds_read_b64 v[134:135], v9
	ds_read_b64 v[136:137], v11
	ds_read_b64 v[138:139], v13
	ds_read_b64 v[140:141], v15
	s_setprio 1
	s_waitcnt lgkmcnt(7)
	v_cvt_pk_f32_fp8_e32 v[142:143], v126
	v_cvt_pk_f32_fp8_sdwa v[144:145], v126 src0_sel:WORD_1
	v_cvt_pk_f32_fp8_e32 v[146:147], v127
	v_cvt_pk_f32_fp8_sdwa v[126:127], v127 src0_sel:WORD_1
	s_waitcnt lgkmcnt(6)
	v_cvt_pk_f32_fp8_e32 v[148:149], v128
	v_cvt_pk_f32_fp8_sdwa v[150:151], v128 src0_sel:WORD_1
	v_cvt_pk_f32_fp8_e32 v[152:153], v129
	v_cvt_pk_f32_fp8_sdwa v[128:129], v129 src0_sel:WORD_1
	s_waitcnt lgkmcnt(5)
	v_cvt_pk_f32_fp8_e32 v[154:155], v130
	v_cvt_pk_f32_fp8_sdwa v[156:157], v130 src0_sel:WORD_1
	v_cvt_pk_f32_fp8_e32 v[158:159], v131
	v_cvt_pk_f32_fp8_sdwa v[130:131], v131 src0_sel:WORD_1
	s_waitcnt lgkmcnt(4)
	v_cvt_pk_f32_fp8_e32 v[160:161], v132
	v_cvt_pk_f32_fp8_sdwa v[162:163], v132 src0_sel:WORD_1
	v_cvt_pk_f32_fp8_e32 v[164:165], v133
	v_cvt_pk_f32_fp8_sdwa v[132:133], v133 src0_sel:WORD_1
	s_waitcnt lgkmcnt(3)
	v_cvt_pk_f32_fp8_e32 v[166:167], v134
	v_cvt_pk_f32_fp8_sdwa v[168:169], v134 src0_sel:WORD_1
	v_cvt_pk_f32_fp8_e32 v[170:171], v135
	v_cvt_pk_f32_fp8_sdwa v[134:135], v135 src0_sel:WORD_1
	s_waitcnt lgkmcnt(2)
	v_cvt_pk_f32_fp8_e32 v[172:173], v136
	v_cvt_pk_f32_fp8_sdwa v[174:175], v136 src0_sel:WORD_1
	v_cvt_pk_f32_fp8_e32 v[176:177], v137
	v_cvt_pk_f32_fp8_sdwa v[136:137], v137 src0_sel:WORD_1
	s_waitcnt lgkmcnt(1)
	v_cvt_pk_f32_fp8_e32 v[178:179], v138
	v_cvt_pk_f32_fp8_sdwa v[180:181], v138 src0_sel:WORD_1
	v_cvt_pk_f32_fp8_e32 v[182:183], v139
	v_cvt_pk_f32_fp8_sdwa v[138:139], v139 src0_sel:WORD_1
	s_waitcnt lgkmcnt(0)
	v_cvt_pk_f32_fp8_e32 v[184:185], v140
	v_cvt_pk_f32_fp8_sdwa v[186:187], v140 src0_sel:WORD_1
	v_cvt_pk_f32_fp8_e32 v[188:189], v141
	v_cvt_pk_f32_fp8_sdwa v[140:141], v141 src0_sel:WORD_1
	s_setprio 0
	s_waitcnt vmcnt(48)
	v_and_b32_e32 v9, 0x1fff8, v52
	v_and_b32_e32 v11, 0x1fff8, v32
	v_and_b32_e32 v13, 0x1fff8, v34
	v_and_b32_e32 v15, 0x1fff8, v36
	ds_read_b64 v[190:191], v9
	ds_read_b64 v[192:193], v11
	ds_read_b64 v[194:195], v13
	ds_read_b64 v[196:197], v15
	v_and_b32_e32 v9, 0x1fff8, v38
	v_and_b32_e32 v11, 0x1fff8, v40
	v_and_b32_e32 v13, 0x1fff8, v42
	v_and_b32_e32 v15, 0x1fff8, v44
	ds_read_b64 v[198:199], v9
	ds_read_b64 v[200:201], v11
	ds_read_b64 v[202:203], v13
	ds_read_b64 v[204:205], v15
	s_setprio 1
	v_pk_fma_f32 v[118:119], v[142:143], v[64:65], v[118:119] op_sel_hi:[1,0,1]
	v_pk_fma_f32 v[122:123], v[144:145], v[64:65], v[122:123] op_sel_hi:[1,0,1]
	v_pk_fma_f32 v[120:121], v[146:147], v[64:65], v[120:121] op_sel_hi:[1,0,1]
	v_pk_fma_f32 v[64:65], v[126:127], v[64:65], v[124:125] op_sel_hi:[1,0,1]
	v_pk_fma_f32 v[118:119], v[148:149], v[66:67], v[118:119] op_sel_hi:[1,0,1]
	v_pk_fma_f32 v[122:123], v[150:151], v[66:67], v[122:123] op_sel_hi:[1,0,1]
	v_pk_fma_f32 v[120:121], v[152:153], v[66:67], v[120:121] op_sel_hi:[1,0,1]
	v_pk_fma_f32 v[64:65], v[128:129], v[66:67], v[64:65] op_sel_hi:[1,0,1]
	v_pk_fma_f32 v[118:119], v[154:155], v[68:69], v[118:119] op_sel_hi:[1,0,1]
	v_pk_fma_f32 v[122:123], v[156:157], v[68:69], v[122:123] op_sel_hi:[1,0,1]
	v_pk_fma_f32 v[120:121], v[158:159], v[68:69], v[120:121] op_sel_hi:[1,0,1]
	v_pk_fma_f32 v[64:65], v[130:131], v[68:69], v[64:65] op_sel_hi:[1,0,1]
	v_pk_fma_f32 v[118:119], v[160:161], v[70:71], v[118:119] op_sel_hi:[1,0,1]
	v_pk_fma_f32 v[122:123], v[162:163], v[70:71], v[122:123] op_sel_hi:[1,0,1]
	v_pk_fma_f32 v[120:121], v[164:165], v[70:71], v[120:121] op_sel_hi:[1,0,1]
	v_pk_fma_f32 v[64:65], v[132:133], v[70:71], v[64:65] op_sel_hi:[1,0,1]
	s_waitcnt lgkmcnt(7)
	v_cvt_pk_f32_fp8_e32 v[206:207], v190
	v_cvt_pk_f32_fp8_sdwa v[208:209], v190 src0_sel:WORD_1
	v_cvt_pk_f32_fp8_e32 v[210:211], v191
	v_cvt_pk_f32_fp8_sdwa v[190:191], v191 src0_sel:WORD_1
	v_pk_fma_f32 v[118:119], v[166:167], v[72:73], v[118:119] op_sel_hi:[1,0,1]
	v_pk_fma_f32 v[122:123], v[168:169], v[72:73], v[122:123] op_sel_hi:[1,0,1]
	v_pk_fma_f32 v[120:121], v[170:171], v[72:73], v[120:121] op_sel_hi:[1,0,1]
	v_pk_fma_f32 v[64:65], v[134:135], v[72:73], v[64:65] op_sel_hi:[1,0,1]
	v_pk_fma_f32 v[118:119], v[172:173], v[74:75], v[118:119] op_sel_hi:[1,0,1]
	v_pk_fma_f32 v[122:123], v[174:175], v[74:75], v[122:123] op_sel_hi:[1,0,1]
	v_pk_fma_f32 v[120:121], v[176:177], v[74:75], v[120:121] op_sel_hi:[1,0,1]
	v_pk_fma_f32 v[64:65], v[136:137], v[74:75], v[64:65] op_sel_hi:[1,0,1]
	s_waitcnt lgkmcnt(6)
	v_cvt_pk_f32_fp8_e32 v[66:67], v192
	v_cvt_pk_f32_fp8_sdwa v[68:69], v192 src0_sel:WORD_1
	v_cvt_pk_f32_fp8_e32 v[70:71], v193
	v_cvt_pk_f32_fp8_sdwa v[72:73], v193 src0_sel:WORD_1
	s_waitcnt lgkmcnt(5)
	v_cvt_pk_f32_fp8_e32 v[74:75], v194
	v_cvt_pk_f32_fp8_sdwa v[124:125], v194 src0_sel:WORD_1
	v_pk_fma_f32 v[118:119], v[178:179], v[48:49], v[118:119] op_sel_hi:[1,0,1]
	v_pk_fma_f32 v[122:123], v[180:181], v[48:49], v[122:123] op_sel_hi:[1,0,1]
	v_pk_fma_f32 v[120:121], v[182:183], v[48:49], v[120:121] op_sel_hi:[1,0,1]
	v_pk_fma_f32 v[48:49], v[138:139], v[48:49], v[64:65] op_sel_hi:[1,0,1]
	v_pk_fma_f32 v[118:119], v[184:185], v[50:51], v[118:119] op_sel_hi:[1,0,1]
	v_pk_fma_f32 v[122:123], v[186:187], v[50:51], v[122:123] op_sel_hi:[1,0,1]
	v_pk_fma_f32 v[120:121], v[188:189], v[50:51], v[120:121] op_sel_hi:[1,0,1]
	v_pk_fma_f32 v[48:49], v[140:141], v[50:51], v[48:49] op_sel_hi:[1,0,1]
	v_pk_fma_f32 v[118:119], v[206:207], v[52:53], v[118:119] op_sel_hi:[1,0,1]
	v_pk_fma_f32 v[122:123], v[208:209], v[52:53], v[122:123] op_sel_hi:[1,0,1]
	v_pk_fma_f32 v[120:121], v[210:211], v[52:53], v[120:121] op_sel_hi:[1,0,1]
	v_pk_fma_f32 v[48:49], v[190:191], v[52:53], v[48:49] op_sel_hi:[1,0,1]
	v_cvt_pk_f32_fp8_e32 v[126:127], v195
	v_cvt_pk_f32_fp8_sdwa v[128:129], v195 src0_sel:WORD_1
	s_waitcnt lgkmcnt(4)
	v_cvt_pk_f32_fp8_e32 v[130:131], v196
	v_cvt_pk_f32_fp8_sdwa v[132:133], v196 src0_sel:WORD_1
	v_cvt_pk_f32_fp8_e32 v[134:135], v197
	v_cvt_pk_f32_fp8_sdwa v[136:137], v197 src0_sel:WORD_1
	s_waitcnt lgkmcnt(3)
	v_cvt_pk_f32_fp8_e32 v[142:143], v198
	v_cvt_pk_f32_fp8_sdwa v[144:145], v198 src0_sel:WORD_1
	v_cvt_pk_f32_fp8_e32 v[146:147], v199
	v_cvt_pk_f32_fp8_sdwa v[148:149], v199 src0_sel:WORD_1
	s_waitcnt lgkmcnt(2)
	v_cvt_pk_f32_fp8_e32 v[150:151], v200
	v_cvt_pk_f32_fp8_sdwa v[152:153], v200 src0_sel:WORD_1
	v_cvt_pk_f32_fp8_e32 v[154:155], v201
	v_cvt_pk_f32_fp8_sdwa v[156:157], v201 src0_sel:WORD_1
	s_waitcnt lgkmcnt(1)
	v_cvt_pk_f32_fp8_e32 v[158:159], v202
	v_cvt_pk_f32_fp8_sdwa v[160:161], v202 src0_sel:WORD_1
	v_cvt_pk_f32_fp8_e32 v[162:163], v203
	v_cvt_pk_f32_fp8_sdwa v[164:165], v203 src0_sel:WORD_1
	s_waitcnt lgkmcnt(0)
	v_cvt_pk_f32_fp8_e32 v[166:167], v204
	v_cvt_pk_f32_fp8_sdwa v[168:169], v204 src0_sel:WORD_1
	v_cvt_pk_f32_fp8_e32 v[170:171], v205
	v_cvt_pk_f32_fp8_sdwa v[172:173], v205 src0_sel:WORD_1
	s_setprio 0
	s_waitcnt vmcnt(40)
	v_and_b32_e32 v9, 0x1fff8, v46
	v_and_b32_e32 v11, 0x1fff8, v26
	v_and_b32_e32 v13, 0x1fff8, v28
	v_and_b32_e32 v15, 0x1fff8, v30
	ds_read_b64 v[50:51], v9
	ds_read_b64 v[52:53], v11
	ds_read_b64 v[64:65], v13
	ds_read_b64 v[138:139], v15
	v_and_b32_e32 v9, 0x1fff8, v4
	v_and_b32_e32 v11, 0x1fff8, v6
	v_and_b32_e32 v13, 0x1fff8, v8
	v_and_b32_e32 v15, 0x1fff8, v10
	ds_read_b64 v[140:141], v9
	ds_read_b64 v[174:175], v11
	ds_read_b64 v[176:177], v13
	ds_read_b64 v[178:179], v15
	s_setprio 1
	v_pk_fma_f32 v[66:67], v[66:67], v[32:33], v[118:119] op_sel_hi:[1,0,1]
	v_pk_fma_f32 v[68:69], v[68:69], v[32:33], v[122:123] op_sel_hi:[1,0,1]
	v_pk_fma_f32 v[70:71], v[70:71], v[32:33], v[120:121] op_sel_hi:[1,0,1]
	v_pk_fma_f32 v[32:33], v[72:73], v[32:33], v[48:49] op_sel_hi:[1,0,1]
	v_pk_fma_f32 v[66:67], v[74:75], v[34:35], v[66:67] op_sel_hi:[1,0,1]
	v_pk_fma_f32 v[68:69], v[124:125], v[34:35], v[68:69] op_sel_hi:[1,0,1]
	v_pk_fma_f32 v[70:71], v[126:127], v[34:35], v[70:71] op_sel_hi:[1,0,1]
	v_pk_fma_f32 v[32:33], v[128:129], v[34:35], v[32:33] op_sel_hi:[1,0,1]
	v_pk_fma_f32 v[66:67], v[130:131], v[36:37], v[66:67] op_sel_hi:[1,0,1]
	v_pk_fma_f32 v[68:69], v[132:133], v[36:37], v[68:69] op_sel_hi:[1,0,1]
	v_pk_fma_f32 v[70:71], v[134:135], v[36:37], v[70:71] op_sel_hi:[1,0,1]
	v_pk_fma_f32 v[32:33], v[136:137], v[36:37], v[32:33] op_sel_hi:[1,0,1]
	s_waitcnt lgkmcnt(7)
	v_cvt_pk_f32_fp8_e32 v[180:181], v50
	v_cvt_pk_f32_fp8_sdwa v[182:183], v50 src0_sel:WORD_1
	v_cvt_pk_f32_fp8_e32 v[184:185], v51
	v_cvt_pk_f32_fp8_sdwa v[50:51], v51 src0_sel:WORD_1
	v_pk_fma_f32 v[66:67], v[142:143], v[38:39], v[66:67] op_sel_hi:[1,0,1]
	v_pk_fma_f32 v[68:69], v[144:145], v[38:39], v[68:69] op_sel_hi:[1,0,1]
	v_pk_fma_f32 v[70:71], v[146:147], v[38:39], v[70:71] op_sel_hi:[1,0,1]
	v_pk_fma_f32 v[32:33], v[148:149], v[38:39], v[32:33] op_sel_hi:[1,0,1]
	s_waitcnt lgkmcnt(6)
	v_cvt_pk_f32_fp8_e32 v[186:187], v52
	v_cvt_pk_f32_fp8_sdwa v[188:189], v52 src0_sel:WORD_1
	v_cvt_pk_f32_fp8_e32 v[190:191], v53
	v_cvt_pk_f32_fp8_sdwa v[52:53], v53 src0_sel:WORD_1
	v_pk_fma_f32 v[66:67], v[150:151], v[40:41], v[66:67] op_sel_hi:[1,0,1]
	v_pk_fma_f32 v[68:69], v[152:153], v[40:41], v[68:69] op_sel_hi:[1,0,1]
	v_pk_fma_f32 v[70:71], v[154:155], v[40:41], v[70:71] op_sel_hi:[1,0,1]
	v_pk_fma_f32 v[32:33], v[156:157], v[40:41], v[32:33] op_sel_hi:[1,0,1]
	s_waitcnt lgkmcnt(5)
	v_cvt_pk_f32_fp8_e32 v[192:193], v64
	v_cvt_pk_f32_fp8_sdwa v[194:195], v64 src0_sel:WORD_1
	v_cvt_pk_f32_fp8_e32 v[196:197], v65
	v_cvt_pk_f32_fp8_sdwa v[64:65], v65 src0_sel:WORD_1
	v_pk_fma_f32 v[66:67], v[158:159], v[42:43], v[66:67] op_sel_hi:[1,0,1]
	v_pk_fma_f32 v[68:69], v[160:161], v[42:43], v[68:69] op_sel_hi:[1,0,1]
	v_pk_fma_f32 v[70:71], v[162:163], v[42:43], v[70:71] op_sel_hi:[1,0,1]
	v_pk_fma_f32 v[32:33], v[164:165], v[42:43], v[32:33] op_sel_hi:[1,0,1]
	s_waitcnt lgkmcnt(4)
	v_cvt_pk_f32_fp8_e32 v[198:199], v138
	v_cvt_pk_f32_fp8_sdwa v[200:201], v138 src0_sel:WORD_1
	v_cvt_pk_f32_fp8_e32 v[202:203], v139
	v_cvt_pk_f32_fp8_sdwa v[138:139], v139 src0_sel:WORD_1
	v_pk_fma_f32 v[66:67], v[166:167], v[44:45], v[66:67] op_sel_hi:[1,0,1]
	v_pk_fma_f32 v[68:69], v[168:169], v[44:45], v[68:69] op_sel_hi:[1,0,1]
	v_pk_fma_f32 v[70:71], v[170:171], v[44:45], v[70:71] op_sel_hi:[1,0,1]
	v_pk_fma_f32 v[32:33], v[172:173], v[44:45], v[32:33] op_sel_hi:[1,0,1]
	v_pk_fma_f32 v[66:67], v[180:181], v[46:47], v[66:67] op_sel_hi:[1,0,1]
	v_pk_fma_f32 v[68:69], v[182:183], v[46:47], v[68:69] op_sel_hi:[1,0,1]
	v_pk_fma_f32 v[70:71], v[184:185], v[46:47], v[70:71] op_sel_hi:[1,0,1]
	v_pk_fma_f32 v[32:33], v[50:51], v[46:47], v[32:33] op_sel_hi:[1,0,1]
	s_waitcnt lgkmcnt(3)
	v_cvt_pk_f32_fp8_e32 v[34:35], v140
	v_cvt_pk_f32_fp8_sdwa v[36:37], v140 src0_sel:WORD_1
	v_cvt_pk_f32_fp8_e32 v[38:39], v141
	v_cvt_pk_f32_fp8_sdwa v[40:41], v141 src0_sel:WORD_1
	s_waitcnt lgkmcnt(2)
	v_cvt_pk_f32_fp8_e32 v[42:43], v174
	v_cvt_pk_f32_fp8_sdwa v[44:45], v174 src0_sel:WORD_1
	v_cvt_pk_f32_fp8_e32 v[46:47], v175
	v_cvt_pk_f32_fp8_sdwa v[48:49], v175 src0_sel:WORD_1
	s_waitcnt lgkmcnt(1)
	v_cvt_pk_f32_fp8_e32 v[50:51], v176
	v_cvt_pk_f32_fp8_sdwa v[72:73], v176 src0_sel:WORD_1
	v_cvt_pk_f32_fp8_e32 v[74:75], v177
	v_cvt_pk_f32_fp8_sdwa v[118:119], v177 src0_sel:WORD_1
	s_waitcnt lgkmcnt(0)
	v_cvt_pk_f32_fp8_e32 v[120:121], v178
	v_cvt_pk_f32_fp8_sdwa v[122:123], v178 src0_sel:WORD_1
	v_cvt_pk_f32_fp8_e32 v[124:125], v179
	v_pk_fma_f32 v[66:67], v[186:187], v[26:27], v[66:67] op_sel_hi:[1,0,1]
	v_pk_fma_f32 v[68:69], v[188:189], v[26:27], v[68:69] op_sel_hi:[1,0,1]
	v_pk_fma_f32 v[70:71], v[190:191], v[26:27], v[70:71] op_sel_hi:[1,0,1]
	v_pk_fma_f32 v[26:27], v[52:53], v[26:27], v[32:33] op_sel_hi:[1,0,1]
	v_pk_fma_f32 v[66:67], v[192:193], v[28:29], v[66:67] op_sel_hi:[1,0,1]
	v_pk_fma_f32 v[68:69], v[194:195], v[28:29], v[68:69] op_sel_hi:[1,0,1]
	v_pk_fma_f32 v[70:71], v[196:197], v[28:29], v[70:71] op_sel_hi:[1,0,1]
	v_pk_fma_f32 v[26:27], v[64:65], v[28:29], v[26:27] op_sel_hi:[1,0,1]
	v_pk_fma_f32 v[66:67], v[198:199], v[30:31], v[66:67] op_sel_hi:[1,0,1]
	v_pk_fma_f32 v[68:69], v[200:201], v[30:31], v[68:69] op_sel_hi:[1,0,1]
	v_pk_fma_f32 v[70:71], v[202:203], v[30:31], v[70:71] op_sel_hi:[1,0,1]
	v_pk_fma_f32 v[26:27], v[138:139], v[30:31], v[26:27] op_sel_hi:[1,0,1]
	v_cvt_pk_f32_fp8_sdwa v[126:127], v179 src0_sel:WORD_1
	s_setprio 0
	s_waitcnt vmcnt(32)
	v_and_b32_e32 v9, 0x1fff8, v14
	v_and_b32_e32 v11, 0x1fff8, v18
	v_and_b32_e32 v13, 0x1fff8, v20
	v_and_b32_e32 v15, 0x1fff8, v22
	ds_read_b64 v[28:29], v9
	ds_read_b64 v[30:31], v11
	ds_read_b64 v[32:33], v13
	ds_read_b64 v[52:53], v15
	v_and_b32_e32 v9, 0x1fff8, v24
	v_and_b32_e32 v11, 0x1fff8, v12
	v_and_b32_e32 v13, 0x1fff8, v16
	v_and_b32_e32 v15, 0x1fff8, v7
	ds_read_b64 v[64:65], v9
	ds_read_b64 v[128:129], v11
	ds_read_b64 v[130:131], v13
	ds_read_b64 v[132:133], v15
	s_setprio 1
	s_waitcnt lgkmcnt(7)
	v_cvt_pk_f32_fp8_e32 v[134:135], v28
	v_pk_fma_f32 v[34:35], v[34:35], v[4:5], v[66:67] op_sel_hi:[1,0,1]
	s_waitcnt lgkmcnt(6)
	v_cvt_pk_f32_fp8_e32 v[140:141], v30
	v_pk_fma_f32 v[34:35], v[42:43], v[6:7], v[34:35] op_sel_hi:[1,0,1]
	s_waitcnt lgkmcnt(5)
	v_cvt_pk_f32_fp8_e32 v[146:147], v32
	v_pk_fma_f32 v[34:35], v[50:51], v[8:9], v[34:35] op_sel_hi:[1,0,1]
	s_waitcnt lgkmcnt(4)
	v_cvt_pk_f32_fp8_e32 v[152:153], v52
	v_pk_fma_f32 v[34:35], v[120:121], v[10:11], v[34:35] op_sel_hi:[1,0,1]
	s_waitcnt lgkmcnt(3)
	v_cvt_pk_f32_fp8_e32 v[158:159], v64
	v_pk_fma_f32 v[34:35], v[134:135], v[14:15], v[34:35] op_sel_hi:[1,0,1]
	s_waitcnt lgkmcnt(2)
	v_cvt_pk_f32_fp8_e32 v[164:165], v128
	v_pk_fma_f32 v[34:35], v[140:141], v[18:19], v[34:35] op_sel_hi:[1,0,1]
	s_waitcnt lgkmcnt(1)
	v_cvt_pk_f32_fp8_e32 v[170:171], v130
	v_pk_fma_f32 v[34:35], v[146:147], v[20:21], v[34:35] op_sel_hi:[1,0,1]
	v_cvt_pk_f32_fp8_sdwa v[136:137], v28 src0_sel:WORD_1
	v_pk_fma_f32 v[34:35], v[152:153], v[22:23], v[34:35] op_sel_hi:[1,0,1]
	v_cvt_pk_f32_fp8_sdwa v[142:143], v30 src0_sel:WORD_1
	v_pk_fma_f32 v[34:35], v[158:159], v[24:25], v[34:35] op_sel_hi:[1,0,1]
	v_cvt_pk_f32_fp8_sdwa v[148:149], v32 src0_sel:WORD_1
	v_pk_fma_f32 v[34:35], v[164:165], v[12:13], v[34:35] op_sel_hi:[1,0,1]
	v_cvt_pk_f32_fp8_sdwa v[154:155], v52 src0_sel:WORD_1
	v_pk_fma_f32 v[120:121], v[170:171], v[16:17], v[34:35] op_sel_hi:[1,0,1]
	v_pk_fma_f32 v[34:35], v[36:37], v[4:5], v[68:69] op_sel_hi:[1,0,1]
	v_cvt_pk_f32_fp8_sdwa v[160:161], v64 src0_sel:WORD_1
	v_pk_fma_f32 v[34:35], v[44:45], v[6:7], v[34:35] op_sel_hi:[1,0,1]
	v_cvt_pk_f32_fp8_sdwa v[166:167], v128 src0_sel:WORD_1
	v_pk_fma_f32 v[34:35], v[72:73], v[8:9], v[34:35] op_sel_hi:[1,0,1]
	v_cvt_pk_f32_fp8_sdwa v[172:173], v130 src0_sel:WORD_1
	v_pk_fma_f32 v[34:35], v[122:123], v[10:11], v[34:35] op_sel_hi:[1,0,1]
	v_cvt_pk_f32_fp8_e32 v[138:139], v29
	v_pk_fma_f32 v[34:35], v[136:137], v[14:15], v[34:35] op_sel_hi:[1,0,1]
	v_cvt_pk_f32_fp8_sdwa v[28:29], v29 src0_sel:WORD_1
	v_pk_fma_f32 v[34:35], v[142:143], v[18:19], v[34:35] op_sel_hi:[1,0,1]
	v_cvt_pk_f32_fp8_e32 v[144:145], v31
	v_pk_fma_f32 v[34:35], v[148:149], v[20:21], v[34:35] op_sel_hi:[1,0,1]
	v_pk_fma_f32 v[26:27], v[40:41], v[4:5], v[26:27] op_sel_hi:[1,0,1]
	v_pk_fma_f32 v[34:35], v[154:155], v[22:23], v[34:35] op_sel_hi:[1,0,1]
	v_cvt_pk_f32_fp8_sdwa v[30:31], v31 src0_sel:WORD_1
	v_pk_fma_f32 v[34:35], v[160:161], v[24:25], v[34:35] op_sel_hi:[1,0,1]
	v_cvt_pk_f32_fp8_e32 v[150:151], v33
	v_pk_fma_f32 v[34:35], v[166:167], v[12:13], v[34:35] op_sel_hi:[1,0,1]
	v_pk_fma_f32 v[26:27], v[48:49], v[6:7], v[26:27] op_sel_hi:[1,0,1]
	v_pk_fma_f32 v[122:123], v[172:173], v[16:17], v[34:35] op_sel_hi:[1,0,1]
	v_pk_fma_f32 v[34:35], v[38:39], v[4:5], v[70:71] op_sel_hi:[1,0,1]
	v_cvt_pk_f32_fp8_sdwa v[32:33], v33 src0_sel:WORD_1
	v_pk_fma_f32 v[34:35], v[46:47], v[6:7], v[34:35] op_sel_hi:[1,0,1]
	v_cvt_pk_f32_fp8_e32 v[156:157], v53
	v_pk_fma_f32 v[34:35], v[74:75], v[8:9], v[34:35] op_sel_hi:[1,0,1]
	v_pk_fma_f32 v[8:9], v[118:119], v[8:9], v[26:27] op_sel_hi:[1,0,1]
	v_pk_fma_f32 v[34:35], v[124:125], v[10:11], v[34:35] op_sel_hi:[1,0,1]
	v_cvt_pk_f32_fp8_sdwa v[52:53], v53 src0_sel:WORD_1
	v_cvt_pk_f32_fp8_e32 v[162:163], v65
	v_pk_fma_f32 v[34:35], v[138:139], v[14:15], v[34:35] op_sel_hi:[1,0,1]
	v_pk_fma_f32 v[8:9], v[126:127], v[10:11], v[8:9] op_sel_hi:[1,0,1]
	v_cvt_pk_f32_fp8_sdwa v[64:65], v65 src0_sel:WORD_1
	v_cvt_pk_f32_fp8_e32 v[168:169], v129
	v_pk_fma_f32 v[34:35], v[144:145], v[18:19], v[34:35] op_sel_hi:[1,0,1]
	v_pk_fma_f32 v[8:9], v[28:29], v[14:15], v[8:9] op_sel_hi:[1,0,1]
	v_cvt_pk_f32_fp8_sdwa v[128:129], v129 src0_sel:WORD_1
	v_cvt_pk_f32_fp8_e32 v[174:175], v131
	v_pk_fma_f32 v[34:35], v[150:151], v[20:21], v[34:35] op_sel_hi:[1,0,1]
	v_pk_fma_f32 v[8:9], v[30:31], v[18:19], v[8:9] op_sel_hi:[1,0,1]
	v_cvt_pk_f32_fp8_sdwa v[130:131], v131 src0_sel:WORD_1
	v_pk_fma_f32 v[34:35], v[156:157], v[22:23], v[34:35] op_sel_hi:[1,0,1]
	v_pk_fma_f32 v[8:9], v[32:33], v[20:21], v[8:9] op_sel_hi:[1,0,1]
	s_waitcnt lgkmcnt(0)
	v_cvt_pk_f32_fp8_e32 v[118:119], v132
	v_pk_fma_f32 v[34:35], v[162:163], v[24:25], v[34:35] op_sel_hi:[1,0,1]
	v_pk_fma_f32 v[8:9], v[52:53], v[22:23], v[8:9] op_sel_hi:[1,0,1]
	v_pk_fma_f32 v[34:35], v[168:169], v[12:13], v[34:35] op_sel_hi:[1,0,1]
	v_pk_fma_f32 v[8:9], v[64:65], v[24:25], v[8:9] op_sel_hi:[1,0,1]
	v_pk_fma_f32 v[124:125], v[174:175], v[16:17], v[34:35] op_sel_hi:[1,0,1]
	v_pk_fma_f32 v[8:9], v[128:129], v[12:13], v[8:9] op_sel_hi:[1,0,1]
	v_cvt_pk_f32_fp8_sdwa v[126:127], v132 src0_sel:WORD_1
	v_cvt_pk_f32_fp8_e32 v[134:135], v133
	v_cvt_pk_f32_fp8_sdwa v[132:133], v133 src0_sel:WORD_1
	v_pk_fma_f32 v[128:129], v[130:131], v[16:17], v[8:9] op_sel_hi:[1,0,1]
	v_mov_b32_e32 v130, v7
	s_setprio 0
	s_add_i32 s18, s18, 2
	s_cmp_gt_u32 s17, 61
	s_cselect_b64 s[10:11], -1, 0
	s_cmp_lt_u32 s17, 62
	s_cselect_b32 s19, s18, 63
	s_lshl_b32 s20, s19, 1
	s_and_b32 s20, s20, 0xf8
	s_add_i32 s20, s20, s4
	s_ashr_i32 s21, s20, 31
	s_lshl_b64 s[20:21], s[20:21], 15
	s_add_u32 s20, s12, s20
	s_addc_u32 s21, s13, s21
	s_lshl_b32 s19, s19, 13
	s_and_b32 s19, s19, 0x6000
	s_add_u32 s20, s20, s19
	s_addc_u32 s21, s21, 0
	s_add_u32 s66, s20, s5
	s_addc_u32 s67, s21, 0
	global_load_dword v64, v2, s[20:21]
	global_load_dword v66, v2, s[20:21] offset:256
	global_load_dword v68, v2, s[20:21] offset:512
	global_load_dword v70, v2, s[20:21] offset:768
	global_load_dword v72, v2, s[20:21] offset:1024
	global_load_dword v74, v2, s[20:21] offset:1280
	global_load_dword v48, v2, s[20:21] offset:1536
	global_load_dword v50, v2, s[20:21] offset:1792
	global_load_dword v52, v2, s[20:21] offset:2048
	global_load_dword v32, v2, s[20:21] offset:2304
	global_load_dword v34, v2, s[20:21] offset:2560
	global_load_dword v36, v2, s[20:21] offset:2816
	global_load_dword v38, v2, s[20:21] offset:3072
	global_load_dword v40, v2, s[20:21] offset:3328
	global_load_dword v42, v2, s[20:21] offset:3584
	global_load_dword v44, v2, s[20:21] offset:3840
	global_load_dword v46, v2, s[66:67]
	global_load_dword v26, v2, s[66:67] offset:256
	global_load_dword v28, v2, s[66:67] offset:512
	global_load_dword v30, v2, s[66:67] offset:768
	global_load_dword v4, v2, s[66:67] offset:1024
	global_load_dword v6, v2, s[66:67] offset:1280
	global_load_dword v8, v2, s[66:67] offset:1536
	global_load_dword v10, v2, s[66:67] offset:1792
	global_load_dword v14, v2, s[66:67] offset:2048
	global_load_dword v18, v2, s[66:67] offset:2304
	global_load_dword v20, v2, s[66:67] offset:2560
	global_load_dword v22, v2, s[66:67] offset:2816
	global_load_dword v24, v2, s[66:67] offset:3072
	global_load_dword v12, v2, s[66:67] offset:3328
	global_load_dword v16, v2, s[66:67] offset:3584
	global_load_dword v7, v2, s[66:67] offset:3840
	s_waitcnt vmcnt(55)
	v_and_b32_e32 v9, 0x1fff8, v116
	v_and_b32_e32 v11, 0x1fff8, v104
	v_and_b32_e32 v13, 0x1fff8, v106
	v_and_b32_e32 v15, 0x1fff8, v108
	ds_read_b64 v[136:137], v9
	ds_read_b64 v[138:139], v11
	ds_read_b64 v[140:141], v13
	ds_read_b64 v[142:143], v15
	v_and_b32_e32 v9, 0x1fff8, v110
	v_and_b32_e32 v11, 0x1fff8, v112
	v_and_b32_e32 v13, 0x1fff8, v114
	v_and_b32_e32 v15, 0x1fff8, v98
	ds_read_b64 v[144:145], v9
	ds_read_b64 v[146:147], v11
	ds_read_b64 v[148:149], v13
	ds_read_b64 v[150:151], v15
	s_setprio 1
	s_waitcnt lgkmcnt(7)
	v_cvt_pk_f32_fp8_e32 v[152:153], v136
	v_cvt_pk_f32_fp8_sdwa v[154:155], v136 src0_sel:WORD_1
	v_cvt_pk_f32_fp8_e32 v[156:157], v137
	v_cvt_pk_f32_fp8_sdwa v[136:137], v137 src0_sel:WORD_1
	s_waitcnt lgkmcnt(6)
	v_cvt_pk_f32_fp8_e32 v[158:159], v138
	v_cvt_pk_f32_fp8_sdwa v[160:161], v138 src0_sel:WORD_1
	v_cvt_pk_f32_fp8_e32 v[162:163], v139
	v_cvt_pk_f32_fp8_sdwa v[138:139], v139 src0_sel:WORD_1
	s_waitcnt lgkmcnt(5)
	v_cvt_pk_f32_fp8_e32 v[164:165], v140
	v_cvt_pk_f32_fp8_sdwa v[166:167], v140 src0_sel:WORD_1
	v_cvt_pk_f32_fp8_e32 v[168:169], v141
	v_cvt_pk_f32_fp8_sdwa v[140:141], v141 src0_sel:WORD_1
	s_waitcnt lgkmcnt(4)
	v_cvt_pk_f32_fp8_e32 v[170:171], v142
	v_cvt_pk_f32_fp8_sdwa v[172:173], v142 src0_sel:WORD_1
	v_cvt_pk_f32_fp8_e32 v[174:175], v143
	v_cvt_pk_f32_fp8_sdwa v[142:143], v143 src0_sel:WORD_1
	s_waitcnt lgkmcnt(3)
	v_cvt_pk_f32_fp8_e32 v[176:177], v144
	v_cvt_pk_f32_fp8_sdwa v[178:179], v144 src0_sel:WORD_1
	v_cvt_pk_f32_fp8_e32 v[180:181], v145
	v_cvt_pk_f32_fp8_sdwa v[144:145], v145 src0_sel:WORD_1
	s_waitcnt lgkmcnt(2)
	v_cvt_pk_f32_fp8_e32 v[182:183], v146
	v_cvt_pk_f32_fp8_sdwa v[184:185], v146 src0_sel:WORD_1
	v_cvt_pk_f32_fp8_e32 v[186:187], v147
	v_cvt_pk_f32_fp8_sdwa v[146:147], v147 src0_sel:WORD_1
	s_waitcnt lgkmcnt(1)
	v_cvt_pk_f32_fp8_e32 v[188:189], v148
	v_cvt_pk_f32_fp8_sdwa v[190:191], v148 src0_sel:WORD_1
	v_cvt_pk_f32_fp8_e32 v[192:193], v149
	v_cvt_pk_f32_fp8_sdwa v[148:149], v149 src0_sel:WORD_1
	s_waitcnt lgkmcnt(0)
	v_cvt_pk_f32_fp8_e32 v[194:195], v150
	v_cvt_pk_f32_fp8_sdwa v[196:197], v150 src0_sel:WORD_1
	v_cvt_pk_f32_fp8_e32 v[198:199], v151
	v_cvt_pk_f32_fp8_sdwa v[150:151], v151 src0_sel:WORD_1
	s_setprio 0
	v_and_b32_e32 v9, 0x1fff8, v100
	s_waitcnt vmcnt(48)
	v_and_b32_e32 v11, 0x1fff8, v102
	v_and_b32_e32 v13, 0x1fff8, v78
	v_and_b32_e32 v15, 0x1fff8, v80
	ds_read_b64 v[200:201], v9
	ds_read_b64 v[202:203], v11
	ds_read_b64 v[204:205], v13
	ds_read_b64 v[206:207], v15
	v_and_b32_e32 v9, 0x1fff8, v82
	v_and_b32_e32 v11, 0x1fff8, v84
	v_and_b32_e32 v13, 0x1fff8, v86
	v_and_b32_e32 v15, 0x1fff8, v88
	ds_read_b64 v[208:209], v9
	ds_read_b64 v[210:211], v11
	ds_read_b64 v[212:213], v13
	ds_read_b64 v[214:215], v15
	s_setprio 1
	v_pk_fma_f32 v[118:119], v[118:119], v[130:131], v[120:121] op_sel_hi:[1,0,1]
	v_pk_fma_f32 v[120:121], v[126:127], v[130:131], v[122:123] op_sel_hi:[1,0,1]
	v_pk_fma_f32 v[122:123], v[134:135], v[130:131], v[124:125] op_sel_hi:[1,0,1]
	v_pk_fma_f32 v[118:119], v[152:153], v[116:117], v[118:119] op_sel_hi:[1,0,1]
	v_pk_fma_f32 v[120:121], v[154:155], v[116:117], v[120:121] op_sel_hi:[1,0,1]
	v_pk_fma_f32 v[122:123], v[156:157], v[116:117], v[122:123] op_sel_hi:[1,0,1]
	v_pk_fma_f32 v[124:125], v[132:133], v[130:131], v[128:129] op_sel_hi:[1,0,1]
	v_pk_fma_f32 v[118:119], v[158:159], v[104:105], v[118:119] op_sel_hi:[1,0,1]
	v_pk_fma_f32 v[120:121], v[160:161], v[104:105], v[120:121] op_sel_hi:[1,0,1]
	v_pk_fma_f32 v[122:123], v[162:163], v[104:105], v[122:123] op_sel_hi:[1,0,1]
	v_pk_fma_f32 v[116:117], v[136:137], v[116:117], v[124:125] op_sel_hi:[1,0,1]
	v_pk_fma_f32 v[118:119], v[164:165], v[106:107], v[118:119] op_sel_hi:[1,0,1]
	v_pk_fma_f32 v[120:121], v[166:167], v[106:107], v[120:121] op_sel_hi:[1,0,1]
	v_pk_fma_f32 v[122:123], v[168:169], v[106:107], v[122:123] op_sel_hi:[1,0,1]
	v_pk_fma_f32 v[104:105], v[138:139], v[104:105], v[116:117] op_sel_hi:[1,0,1]
	v_pk_fma_f32 v[118:119], v[170:171], v[108:109], v[118:119] op_sel_hi:[1,0,1]
	v_pk_fma_f32 v[120:121], v[172:173], v[108:109], v[120:121] op_sel_hi:[1,0,1]
	v_pk_fma_f32 v[122:123], v[174:175], v[108:109], v[122:123] op_sel_hi:[1,0,1]
	v_pk_fma_f32 v[104:105], v[140:141], v[106:107], v[104:105] op_sel_hi:[1,0,1]
	s_waitcnt lgkmcnt(7)
	v_cvt_pk_f32_fp8_e32 v[216:217], v200
	v_cvt_pk_f32_fp8_sdwa v[218:219], v200 src0_sel:WORD_1
	v_cvt_pk_f32_fp8_e32 v[220:221], v201
	v_pk_fma_f32 v[118:119], v[176:177], v[110:111], v[118:119] op_sel_hi:[1,0,1]
	v_pk_fma_f32 v[120:121], v[178:179], v[110:111], v[120:121] op_sel_hi:[1,0,1]
	v_pk_fma_f32 v[122:123], v[180:181], v[110:111], v[122:123] op_sel_hi:[1,0,1]
	v_pk_fma_f32 v[104:105], v[142:143], v[108:109], v[104:105] op_sel_hi:[1,0,1]
	v_cvt_pk_f32_fp8_sdwa v[200:201], v201 src0_sel:WORD_1
	s_waitcnt lgkmcnt(6)
	v_cvt_pk_f32_fp8_e32 v[222:223], v202
	v_cvt_pk_f32_fp8_sdwa v[224:225], v202 src0_sel:WORD_1
	v_cvt_pk_f32_fp8_e32 v[226:227], v203
	v_pk_fma_f32 v[118:119], v[182:183], v[112:113], v[118:119] op_sel_hi:[1,0,1]
	v_pk_fma_f32 v[120:121], v[184:185], v[112:113], v[120:121] op_sel_hi:[1,0,1]
	v_pk_fma_f32 v[122:123], v[186:187], v[112:113], v[122:123] op_sel_hi:[1,0,1]
	v_pk_fma_f32 v[104:105], v[144:145], v[110:111], v[104:105] op_sel_hi:[1,0,1]
	v_cvt_pk_f32_fp8_sdwa v[202:203], v203 src0_sel:WORD_1
	v_pk_fma_f32 v[118:119], v[188:189], v[114:115], v[118:119] op_sel_hi:[1,0,1]
	v_pk_fma_f32 v[120:121], v[190:191], v[114:115], v[120:121] op_sel_hi:[1,0,1]
	v_pk_fma_f32 v[122:123], v[192:193], v[114:115], v[122:123] op_sel_hi:[1,0,1]
	v_pk_fma_f32 v[104:105], v[146:147], v[112:113], v[104:105] op_sel_hi:[1,0,1]
	s_waitcnt lgkmcnt(4)
	v_cvt_pk_f32_fp8_e32 v[124:125], v207
	v_pk_fma_f32 v[118:119], v[194:195], v[98:99], v[118:119] op_sel_hi:[1,0,1]
	v_pk_fma_f32 v[120:121], v[196:197], v[98:99], v[120:121] op_sel_hi:[1,0,1]
	v_pk_fma_f32 v[122:123], v[198:199], v[98:99], v[122:123] op_sel_hi:[1,0,1]
	v_pk_fma_f32 v[104:105], v[148:149], v[114:115], v[104:105] op_sel_hi:[1,0,1]
	v_pk_fma_f32 v[118:119], v[216:217], v[100:101], v[118:119] op_sel_hi:[1,0,1]
	v_pk_fma_f32 v[120:121], v[218:219], v[100:101], v[120:121] op_sel_hi:[1,0,1]
	v_pk_fma_f32 v[122:123], v[220:221], v[100:101], v[122:123] op_sel_hi:[1,0,1]
	v_pk_fma_f32 v[98:99], v[150:151], v[98:99], v[104:105] op_sel_hi:[1,0,1]
	v_pk_fma_f32 v[118:119], v[222:223], v[102:103], v[118:119] op_sel_hi:[1,0,1]
	v_pk_fma_f32 v[120:121], v[224:225], v[102:103], v[120:121] op_sel_hi:[1,0,1]
	v_pk_fma_f32 v[122:123], v[226:227], v[102:103], v[122:123] op_sel_hi:[1,0,1]
	v_pk_fma_f32 v[98:99], v[200:201], v[100:101], v[98:99] op_sel_hi:[1,0,1]
	v_cvt_pk_f32_fp8_e32 v[106:107], v204
	v_cvt_pk_f32_fp8_sdwa v[108:109], v204 src0_sel:WORD_1
	v_cvt_pk_f32_fp8_e32 v[110:111], v205
	v_cvt_pk_f32_fp8_sdwa v[112:113], v205 src0_sel:WORD_1
	v_cvt_pk_f32_fp8_e32 v[114:115], v206
	v_cvt_pk_f32_fp8_sdwa v[116:117], v206 src0_sel:WORD_1
	v_cvt_pk_f32_fp8_sdwa v[126:127], v207 src0_sel:WORD_1
	s_waitcnt lgkmcnt(3)
	v_cvt_pk_f32_fp8_e32 v[128:129], v208
	v_cvt_pk_f32_fp8_sdwa v[130:131], v208 src0_sel:WORD_1
	v_cvt_pk_f32_fp8_e32 v[132:133], v209
	v_cvt_pk_f32_fp8_sdwa v[134:135], v209 src0_sel:WORD_1
	s_waitcnt lgkmcnt(2)
	v_cvt_pk_f32_fp8_e32 v[136:137], v210
	v_cvt_pk_f32_fp8_sdwa v[138:139], v210 src0_sel:WORD_1
	v_cvt_pk_f32_fp8_e32 v[140:141], v211
	v_cvt_pk_f32_fp8_sdwa v[142:143], v211 src0_sel:WORD_1
	s_waitcnt lgkmcnt(1)
	v_cvt_pk_f32_fp8_e32 v[144:145], v212
	v_cvt_pk_f32_fp8_sdwa v[146:147], v212 src0_sel:WORD_1
	v_cvt_pk_f32_fp8_e32 v[148:149], v213
	v_cvt_pk_f32_fp8_sdwa v[152:153], v213 src0_sel:WORD_1
	s_waitcnt lgkmcnt(0)
	v_cvt_pk_f32_fp8_e32 v[154:155], v214
	v_cvt_pk_f32_fp8_sdwa v[156:157], v214 src0_sel:WORD_1
	v_cvt_pk_f32_fp8_e32 v[158:159], v215
	v_cvt_pk_f32_fp8_sdwa v[160:161], v215 src0_sel:WORD_1
	v_pk_fma_f32 v[98:99], v[202:203], v[102:103], v[98:99] op_sel_hi:[1,0,1]
	s_setprio 0
	s_waitcnt vmcnt(40)
	v_and_b32_e32 v9, 0x1fff8, v90
	v_and_b32_e32 v11, 0x1fff8, v92
	v_and_b32_e32 v13, 0x1fff8, v94
	v_and_b32_e32 v15, 0x1fff8, v96
	ds_read_b64 v[100:101], v9
	ds_read_b64 v[102:103], v11
	ds_read_b64 v[104:105], v13
	ds_read_b64 v[150:151], v15
	v_and_b32_e32 v9, 0x1fff8, v76
	v_and_b32_e32 v11, 0x1fff8, v77
	v_and_b32_e32 v13, 0x1fff8, v56
	v_and_b32_e32 v15, 0x1fff8, v57
	ds_read_b64 v[162:163], v9
	ds_read_b64 v[164:165], v11
	ds_read_b64 v[166:167], v13
	ds_read_b64 v[168:169], v15
	s_setprio 1
	v_pk_fma_f32 v[106:107], v[106:107], v[78:79], v[118:119] op_sel_hi:[1,0,1]
	v_pk_fma_f32 v[108:109], v[108:109], v[78:79], v[120:121] op_sel_hi:[1,0,1]
	v_pk_fma_f32 v[110:111], v[110:111], v[78:79], v[122:123] op_sel_hi:[1,0,1]
	v_pk_fma_f32 v[78:79], v[112:113], v[78:79], v[98:99] op_sel_hi:[1,0,1]
	v_pk_fma_f32 v[106:107], v[114:115], v[80:81], v[106:107] op_sel_hi:[1,0,1]
	v_pk_fma_f32 v[108:109], v[116:117], v[80:81], v[108:109] op_sel_hi:[1,0,1]
	v_pk_fma_f32 v[110:111], v[124:125], v[80:81], v[110:111] op_sel_hi:[1,0,1]
	v_pk_fma_f32 v[78:79], v[126:127], v[80:81], v[78:79] op_sel_hi:[1,0,1]
	s_waitcnt lgkmcnt(7)
	v_cvt_pk_f32_fp8_e32 v[170:171], v100
	v_cvt_pk_f32_fp8_sdwa v[172:173], v100 src0_sel:WORD_1
	v_cvt_pk_f32_fp8_e32 v[174:175], v101
	v_cvt_pk_f32_fp8_sdwa v[100:101], v101 src0_sel:WORD_1
	v_pk_fma_f32 v[106:107], v[128:129], v[82:83], v[106:107] op_sel_hi:[1,0,1]
	v_pk_fma_f32 v[108:109], v[130:131], v[82:83], v[108:109] op_sel_hi:[1,0,1]
	v_pk_fma_f32 v[110:111], v[132:133], v[82:83], v[110:111] op_sel_hi:[1,0,1]
	v_pk_fma_f32 v[78:79], v[134:135], v[82:83], v[78:79] op_sel_hi:[1,0,1]
	s_waitcnt lgkmcnt(6)
	v_cvt_pk_f32_fp8_e32 v[176:177], v102
	v_cvt_pk_f32_fp8_sdwa v[178:179], v102 src0_sel:WORD_1
	v_cvt_pk_f32_fp8_e32 v[180:181], v103
	v_cvt_pk_f32_fp8_sdwa v[102:103], v103 src0_sel:WORD_1
	v_pk_fma_f32 v[106:107], v[136:137], v[84:85], v[106:107] op_sel_hi:[1,0,1]
	v_pk_fma_f32 v[108:109], v[138:139], v[84:85], v[108:109] op_sel_hi:[1,0,1]
	v_pk_fma_f32 v[110:111], v[140:141], v[84:85], v[110:111] op_sel_hi:[1,0,1]
	v_pk_fma_f32 v[78:79], v[142:143], v[84:85], v[78:79] op_sel_hi:[1,0,1]
	s_waitcnt lgkmcnt(5)
	v_cvt_pk_f32_fp8_e32 v[182:183], v104
	v_cvt_pk_f32_fp8_sdwa v[184:185], v104 src0_sel:WORD_1
	v_cvt_pk_f32_fp8_e32 v[186:187], v105
	v_cvt_pk_f32_fp8_sdwa v[104:105], v105 src0_sel:WORD_1
	v_pk_fma_f32 v[106:107], v[144:145], v[86:87], v[106:107] op_sel_hi:[1,0,1]
	v_pk_fma_f32 v[108:109], v[146:147], v[86:87], v[108:109] op_sel_hi:[1,0,1]
	v_pk_fma_f32 v[110:111], v[148:149], v[86:87], v[110:111] op_sel_hi:[1,0,1]
	v_pk_fma_f32 v[78:79], v[152:153], v[86:87], v[78:79] op_sel_hi:[1,0,1]
	v_pk_fma_f32 v[106:107], v[154:155], v[88:89], v[106:107] op_sel_hi:[1,0,1]
	v_pk_fma_f32 v[108:109], v[156:157], v[88:89], v[108:109] op_sel_hi:[1,0,1]
	v_pk_fma_f32 v[110:111], v[158:159], v[88:89], v[110:111] op_sel_hi:[1,0,1]
	v_pk_fma_f32 v[78:79], v[160:161], v[88:89], v[78:79] op_sel_hi:[1,0,1]
	s_waitcnt lgkmcnt(3)
	v_cvt_pk_f32_fp8_e32 v[194:195], v162
	v_cvt_pk_f32_fp8_sdwa v[196:197], v162 src0_sel:WORD_1
	v_cvt_pk_f32_fp8_e32 v[198:199], v163
	v_cvt_pk_f32_fp8_sdwa v[162:163], v163 src0_sel:WORD_1
	s_waitcnt lgkmcnt(2)
	v_cvt_pk_f32_fp8_e32 v[200:201], v164
	v_cvt_pk_f32_fp8_sdwa v[202:203], v164 src0_sel:WORD_1
	v_cvt_pk_f32_fp8_e32 v[204:205], v165
	v_cvt_pk_f32_fp8_sdwa v[164:165], v165 src0_sel:WORD_1
	v_pk_fma_f32 v[106:107], v[170:171], v[90:91], v[106:107] op_sel_hi:[1,0,1]
	v_pk_fma_f32 v[108:109], v[172:173], v[90:91], v[108:109] op_sel_hi:[1,0,1]
	v_pk_fma_f32 v[110:111], v[174:175], v[90:91], v[110:111] op_sel_hi:[1,0,1]
	v_pk_fma_f32 v[78:79], v[100:101], v[90:91], v[78:79] op_sel_hi:[1,0,1]
	v_pk_fma_f32 v[106:107], v[176:177], v[92:93], v[106:107] op_sel_hi:[1,0,1]
	v_pk_fma_f32 v[108:109], v[178:179], v[92:93], v[108:109] op_sel_hi:[1,0,1]
	v_pk_fma_f32 v[110:111], v[180:181], v[92:93], v[110:111] op_sel_hi:[1,0,1]
	v_pk_fma_f32 v[78:79], v[102:103], v[92:93], v[78:79] op_sel_hi:[1,0,1]
	v_cvt_pk_f32_fp8_e32 v[188:189], v150
	v_cvt_pk_f32_fp8_sdwa v[190:191], v150 src0_sel:WORD_1
	v_cvt_pk_f32_fp8_e32 v[192:193], v151
	v_cvt_pk_f32_fp8_sdwa v[150:151], v151 src0_sel:WORD_1
	v_pk_fma_f32 v[106:107], v[182:183], v[94:95], v[106:107] op_sel_hi:[1,0,1]
	v_pk_fma_f32 v[108:109], v[184:185], v[94:95], v[108:109] op_sel_hi:[1,0,1]
	v_pk_fma_f32 v[110:111], v[186:187], v[94:95], v[110:111] op_sel_hi:[1,0,1]
	v_pk_fma_f32 v[78:79], v[104:105], v[94:95], v[78:79] op_sel_hi:[1,0,1]
	s_waitcnt lgkmcnt(1)
	v_cvt_pk_f32_fp8_sdwa v[88:89], v167 src0_sel:WORD_1
	s_waitcnt lgkmcnt(0)
	v_cvt_pk_f32_fp8_sdwa v[94:95], v169 src0_sel:WORD_1
	v_pk_fma_f32 v[78:79], v[162:163], v[76:77], v[78:79] op_sel_hi:[1,0,1]
	v_pk_fma_f32 v[106:107], v[188:189], v[96:97], v[106:107] op_sel_hi:[1,0,1]
	v_pk_fma_f32 v[108:109], v[190:191], v[96:97], v[108:109] op_sel_hi:[1,0,1]
	v_pk_fma_f32 v[110:111], v[192:193], v[96:97], v[110:111] op_sel_hi:[1,0,1]
	v_pk_fma_f32 v[78:79], v[150:151], v[96:97], v[78:79] op_sel_hi:[1,0,1]
	v_pk_fma_f32 v[78:79], v[88:89], v[56:57], v[78:79] op_sel_hi:[1,0,1]
	v_pk_fma_f32 v[106:107], v[194:195], v[76:77], v[106:107] op_sel_hi:[1,0,1]
	v_pk_fma_f32 v[108:109], v[196:197], v[76:77], v[108:109] op_sel_hi:[1,0,1]
	v_pk_fma_f32 v[110:111], v[198:199], v[76:77], v[110:111] op_sel_hi:[1,0,1]
	v_pk_fma_f32 v[78:79], v[164:165], v[76:77], v[78:79] op_sel:[0,1,0] op_sel_hi:[1,1,1]
	v_cvt_pk_f32_fp8_e32 v[82:83], v166
	v_cvt_pk_f32_fp8_sdwa v[84:85], v166 src0_sel:WORD_1
	v_cvt_pk_f32_fp8_e32 v[86:87], v167
	v_cvt_pk_f32_fp8_e32 v[90:91], v168
	v_cvt_pk_f32_fp8_sdwa v[92:93], v168 src0_sel:WORD_1
	v_cvt_pk_f32_fp8_e32 v[96:97], v169
	v_pk_fma_f32 v[78:79], v[94:95], v[56:57], v[78:79] op_sel:[0,1,0] op_sel_hi:[1,1,1]
	s_setprio 0
	s_waitcnt vmcnt(32)
	v_and_b32_e32 v9, 0x1fff8, v58
	v_and_b32_e32 v11, 0x1fff8, v59
	v_and_b32_e32 v13, 0x1fff8, v60
	v_and_b32_e32 v15, 0x1fff8, v61
	ds_read_b64 v[100:101], v9
	ds_read_b64 v[102:103], v11
	ds_read_b64 v[104:105], v13
	ds_read_b64 v[112:113], v15
	v_and_b32_e32 v9, 0x1fff8, v62
	v_and_b32_e32 v11, 0x1fff8, v63
	v_and_b32_e32 v13, 0x1fff8, v54
	v_and_b32_e32 v15, 0x1fff8, v55
	ds_read_b64 v[114:115], v9
	ds_read_b64 v[118:119], v11
	ds_read_b64 v[120:121], v13
	ds_read_b64 v[122:123], v15
	s_setprio 1
	s_waitcnt lgkmcnt(7)
	v_cvt_pk_f32_fp8_e32 v[124:125], v100
	v_cvt_pk_f32_fp8_sdwa v[126:127], v100 src0_sel:WORD_1
	v_cvt_pk_f32_fp8_e32 v[128:129], v101
	v_cvt_pk_f32_fp8_sdwa v[100:101], v101 src0_sel:WORD_1
	s_waitcnt lgkmcnt(6)
	v_cvt_pk_f32_fp8_sdwa v[134:135], v103 src0_sel:WORD_1
	v_cvt_pk_f32_fp8_e32 v[130:131], v102
	s_waitcnt lgkmcnt(5)
	v_cvt_pk_f32_fp8_e32 v[138:139], v104
	v_cvt_pk_f32_fp8_sdwa v[140:141], v104 src0_sel:WORD_1
	v_cvt_pk_f32_fp8_e32 v[142:143], v105
	v_cvt_pk_f32_fp8_sdwa v[104:105], v105 src0_sel:WORD_1
	s_waitcnt lgkmcnt(4)
	v_cvt_pk_f32_fp8_sdwa v[148:149], v113 src0_sel:WORD_1
	v_pk_fma_f32 v[106:107], v[200:201], v[76:77], v[106:107] op_sel:[0,1,0] op_sel_hi:[1,1,1]
	s_waitcnt lgkmcnt(3)
	v_cvt_pk_f32_fp8_e32 v[152:153], v114
	v_cvt_pk_f32_fp8_sdwa v[154:155], v114 src0_sel:WORD_1
	v_cvt_pk_f32_fp8_e32 v[156:157], v115
	v_cvt_pk_f32_fp8_sdwa v[114:115], v115 src0_sel:WORD_1
	s_waitcnt lgkmcnt(2)
	v_cvt_pk_f32_fp8_sdwa v[162:163], v119 src0_sel:WORD_1
	v_pk_fma_f32 v[82:83], v[82:83], v[56:57], v[106:107] op_sel_hi:[1,0,1]
	v_cvt_pk_f32_fp8_e32 v[144:145], v112
	v_cvt_pk_f32_fp8_e32 v[158:159], v118
	v_cvt_pk_f32_fp8_sdwa v[160:161], v118 src0_sel:WORD_1
	v_cvt_pk_f32_fp8_e32 v[164:165], v119
	s_waitcnt lgkmcnt(1)
	v_cvt_pk_f32_fp8_e32 v[118:119], v120
	v_cvt_pk_f32_fp8_sdwa v[168:169], v120 src0_sel:WORD_1
	v_cvt_pk_f32_fp8_e32 v[170:171], v121
	v_cvt_pk_f32_fp8_sdwa v[120:121], v121 src0_sel:WORD_1
	s_waitcnt lgkmcnt(0)
; #define GAS __attribute__((address_space(1)))
; __device__ __forceinline__ unsigned f2bf(float f) { unsigned u = __builtin_bit_cast(unsigned, f); return (u + 0x7fffu + ((u >> 16) & 1u)) >> 16; }
; template <int VVAR> __device__ __forceinline__ void peer_v_phase(LAS unsigned char* lds, int wave, int vcu, const unsigned char* __restrict__ VS_l, const unsigned* __restrict__ PW, bf16* __restrict__ Y) {
;     ...
; #pragma unroll 1
;     for (int it = 0; it < (VVAR == 5 ? 2 : 64); it += 2) {
;         V_HALF(pa, pb, it + 1);
;         V_HALF(pb, pa, it + 2);
;         if ((it & 3) == 2) {
;             const int blk = th * 128 + wave + 8 * (it >> 2);
;             bf16* yp = Y + ((size_t)blk * 1024 + cs * 8) * 64 + lane;
; #pragma unroll
;             for (int c = 0; c < 8; ++c) ((GAS unsigned short*)yp)[c * 64] = (unsigned short)f2bf(acc[c]);
; #pragma unroll
;             for (int c = 0; c < 8; ++c) acc[c] = 0.f;
;         }
	v_cvt_pk_f32_fp8_sdwa v[176:177], v123 src0_sel:WORD_1
	v_pk_fma_f32 v[82:83], v[90:91], v[56:57], v[82:83] op_sel:[0,1,0] op_sel_hi:[1,1,1]
	v_pk_fma_f32 v[78:79], v[100:101], v[58:59], v[78:79] op_sel_hi:[1,0,1]
	v_pk_fma_f32 v[78:79], v[134:135], v[58:59], v[78:79] op_sel:[0,1,0] op_sel_hi:[1,1,1]
	v_pk_fma_f32 v[82:83], v[124:125], v[58:59], v[82:83] op_sel_hi:[1,0,1]
	v_pk_fma_f32 v[78:79], v[104:105], v[60:61], v[78:79] op_sel_hi:[1,0,1]
	v_pk_fma_f32 v[78:79], v[148:149], v[60:61], v[78:79] op_sel:[0,1,0] op_sel_hi:[1,1,1]
	v_pk_fma_f32 v[82:83], v[130:131], v[58:59], v[82:83] op_sel:[0,1,0] op_sel_hi:[1,1,1]
	v_pk_fma_f32 v[78:79], v[114:115], v[62:63], v[78:79] op_sel_hi:[1,0,1]
	v_pk_fma_f32 v[78:79], v[162:163], v[62:63], v[78:79] op_sel:[0,1,0] op_sel_hi:[1,1,1]
	v_pk_fma_f32 v[82:83], v[138:139], v[60:61], v[82:83] op_sel_hi:[1,0,1]
	v_cvt_pk_f32_fp8_e32 v[172:173], v122
	v_pk_fma_f32 v[78:79], v[120:121], v[54:55], v[78:79] op_sel_hi:[1,0,1]
	v_pk_fma_f32 v[82:83], v[144:145], v[60:61], v[82:83] op_sel:[0,1,0] op_sel_hi:[1,1,1]
	v_pk_fma_f32 v[124:125], v[176:177], v[54:55], v[78:79] op_sel:[0,1,0] op_sel_hi:[1,1,1]
	v_pk_fma_f32 v[82:83], v[152:153], v[62:63], v[82:83] op_sel_hi:[1,0,1]
	v_pk_fma_f32 v[82:83], v[158:159], v[62:63], v[82:83] op_sel:[0,1,0] op_sel_hi:[1,1,1]
	v_pk_fma_f32 v[82:83], v[118:119], v[54:55], v[82:83] op_sel_hi:[1,0,1]
	v_cvt_pk_f32_fp8_sdwa v[132:133], v102 src0_sel:WORD_1
	v_cvt_pk_f32_fp8_e32 v[102:103], v103
	v_pk_fma_f32 v[118:119], v[172:173], v[54:55], v[82:83] op_sel:[0,1,0] op_sel_hi:[1,1,1]
	v_pk_fma_f32 v[82:83], v[202:203], v[76:77], v[108:109] op_sel:[0,1,0] op_sel_hi:[1,1,1]
	v_pk_fma_f32 v[76:77], v[204:205], v[76:77], v[110:111] op_sel:[0,1,0] op_sel_hi:[1,1,1]
	v_pk_fma_f32 v[82:83], v[84:85], v[56:57], v[82:83] op_sel_hi:[1,0,1]
	v_pk_fma_f32 v[228:229], v[86:87], v[56:57], v[76:77] op_sel_hi:[1,0,1]
	v_cvt_pk_f32_fp8_sdwa v[146:147], v112 src0_sel:WORD_1
	v_cvt_pk_f32_fp8_e32 v[112:113], v113
	v_pk_fma_f32 v[228:229], v[96:97], v[56:57], v[228:229] op_sel:[0,1,0] op_sel_hi:[1,1,1]
	v_pk_fma_f32 v[82:83], v[92:93], v[56:57], v[82:83] op_sel:[0,1,0] op_sel_hi:[1,1,1]
	v_pk_fma_f32 v[228:229], v[128:129], v[58:59], v[228:229] op_sel_hi:[1,0,1]
	v_pk_fma_f32 v[82:83], v[126:127], v[58:59], v[82:83] op_sel_hi:[1,0,1]
	v_pk_fma_f32 v[228:229], v[102:103], v[58:59], v[228:229] op_sel:[0,1,0] op_sel_hi:[1,1,1]
	v_cvt_pk_f32_fp8_e32 v[178:179], v123
	v_pk_fma_f32 v[228:229], v[142:143], v[60:61], v[228:229] op_sel_hi:[1,0,1]
	v_pk_fma_f32 v[82:83], v[132:133], v[58:59], v[82:83] op_sel:[0,1,0] op_sel_hi:[1,1,1]
	v_pk_fma_f32 v[228:229], v[112:113], v[60:61], v[228:229] op_sel:[0,1,0] op_sel_hi:[1,1,1]
	v_pk_fma_f32 v[82:83], v[140:141], v[60:61], v[82:83] op_sel_hi:[1,0,1]
	v_pk_fma_f32 v[228:229], v[156:157], v[62:63], v[228:229] op_sel_hi:[1,0,1]
	v_pk_fma_f32 v[82:83], v[146:147], v[60:61], v[82:83] op_sel:[0,1,0] op_sel_hi:[1,1,1]
	v_pk_fma_f32 v[228:229], v[164:165], v[62:63], v[228:229] op_sel:[0,1,0] op_sel_hi:[1,1,1]
	v_pk_fma_f32 v[82:83], v[154:155], v[62:63], v[82:83] op_sel_hi:[1,0,1]
	v_pk_fma_f32 v[228:229], v[170:171], v[54:55], v[228:229] op_sel_hi:[1,0,1]
	v_pk_fma_f32 v[82:83], v[160:161], v[62:63], v[82:83] op_sel:[0,1,0] op_sel_hi:[1,1,1]
	v_pk_fma_f32 v[120:121], v[178:179], v[54:55], v[228:229] op_sel:[0,1,0] op_sel_hi:[1,1,1]
	v_cvt_pk_f32_fp8_sdwa v[174:175], v122 src0_sel:WORD_1
	v_pk_fma_f32 v[82:83], v[168:169], v[54:55], v[82:83] op_sel_hi:[1,0,1]
	v_pk_fma_f32 v[122:123], v[174:175], v[54:55], v[82:83] op_sel:[0,1,0] op_sel_hi:[1,1,1]
	s_setprio 0
	s_bitcmp0_b32 s17, 1
	s_cbranch_scc1 .LBB0_955
	s_lshl_b64 s[8:9], s[8:9], 17
	v_lshl_add_u64 v[54:55], v[0:1], 0, s[8:9]
	v_cvt_pk_bf16_f32 v9, v118, v119
	v_cvt_pk_bf16_f32 v11, v122, v123
	v_cvt_pk_bf16_f32 v13, v120, v121
	v_cvt_pk_bf16_f32 v15, v124, v125
	global_store_short v[54:55], v9, off sc0 sc1
	global_store_short_d16_hi v[54:55], v9, off offset:128 sc0 sc1
	global_store_short v[54:55], v11, off offset:256 sc0 sc1
	global_store_short_d16_hi v[54:55], v11, off offset:384 sc0 sc1
	global_store_short v[54:55], v13, off offset:512 sc0 sc1
	global_store_short_d16_hi v[54:55], v13, off offset:640 sc0 sc1
	global_store_short v[54:55], v15, off offset:768 sc0 sc1
	global_store_short_d16_hi v[54:55], v15, off offset:896 sc0 sc1
	v_mov_b64_e32 v[118:119], 0
	v_mov_b64_e32 v[122:123], 0
	v_mov_b64_e32 v[120:121], 0
	v_mov_b64_e32 v[124:125], 0
	s_branch .LBB0_955
